# attention output tail: permlane32_swap pairs + 4 dwordx4 stores instead of 8 dwordx2 half-row stores (docs 7.3 store widening), packed scaling
# speedup vs baseline: 1.0013x; 1.0013x over previous
.LBB0_316:
	ds_read2_b32 v[48:49], v212 offset0:128 offset1:129
	ds_read2_b32 v[46:47], v212 offset0:130 offset1:131
	ds_read2_b32 v[44:45], v212 offset0:136 offset1:137
	ds_read2_b32 v[42:43], v212 offset0:138 offset1:139
	ds_read2_b32 v[40:41], v212 offset0:144 offset1:145
	s_waitcnt lgkmcnt(4)
	s_nop 2
	v_fmamk_f32 v48, v2, 0x3fb8aa3b, v48
	v_fmac_f32_e32 v49, 0x3fb8aa3b, v3
	v_max3_f32 v2, v227, v48, v49
	s_waitcnt lgkmcnt(3)
	v_fmamk_f32 v66, v4, 0x3fb8aa3b, v46
	v_fmac_f32_e32 v47, 0x3fb8aa3b, v5
	v_max3_f32 v2, v2, v66, v47
	s_waitcnt lgkmcnt(2)
	v_fmamk_f32 v46, v6, 0x3fb8aa3b, v44
	v_fmac_f32_e32 v45, 0x3fb8aa3b, v7
	ds_read2_b32 v[38:39], v212 offset0:146 offset1:147
	ds_read2_b32 v[36:37], v212 offset0:152 offset1:153
	ds_read2_b32 v[34:35], v212 offset0:154 offset1:155
	v_max3_f32 v2, v2, v46, v45
	s_waitcnt lgkmcnt(4)
	v_fmamk_f32 v44, v8, 0x3fb8aa3b, v42
	v_fmac_f32_e32 v43, 0x3fb8aa3b, v9
	v_max3_f32 v2, v2, v44, v43
	s_waitcnt lgkmcnt(3)
	v_fmamk_f32 v42, v10, 0x3fb8aa3b, v40
	v_fmac_f32_e32 v41, 0x3fb8aa3b, v11
	v_max3_f32 v2, v2, v42, v41
	s_waitcnt lgkmcnt(2)
	v_fmamk_f32 v40, v12, 0x3fb8aa3b, v38
	v_fmac_f32_e32 v39, 0x3fb8aa3b, v13
	v_max3_f32 v2, v2, v40, v39
	s_waitcnt lgkmcnt(1)
	v_fmamk_f32 v38, v14, 0x3fb8aa3b, v36
	v_fmac_f32_e32 v37, 0x3fb8aa3b, v15
	v_max3_f32 v2, v2, v38, v37
	s_waitcnt lgkmcnt(0)
	v_fmamk_f32 v36, v16, 0x3fb8aa3b, v34
	v_fmac_f32_e32 v35, 0x3fb8aa3b, v17
	v_max3_f32 v2, v2, v36, v35
	ds_bpermute_b32 v3, v129, v2
	s_xor_b64 s[22:23], s[80:81], -1
	s_mov_b64 s[80:81], 0
	s_waitcnt lgkmcnt(0)
	v_max_f32_e32 v3, v3, v3
	v_max_f32_e32 v34, v2, v3
	v_sub_f32_e32 v2, v200, v34
	v_exp_f32_e32 v2, v2
	v_sub_f32_e32 v3, v201, v34
	v_exp_f32_e32 v3, v3
	v_sub_f32_e32 v4, v198, v34
	v_exp_f32_e32 v4, v4
	v_sub_f32_e32 v6, v199, v34
	v_exp_f32_e32 v6, v6
	v_sub_f32_e32 v7, v194, v34
	v_add_f32_e32 v5, 0, v2
	v_exp_f32_e32 v7, v7
	v_sub_f32_e32 v8, v195, v34
	v_add_f32_e32 v5, v3, v5
	v_exp_f32_e32 v8, v8
	v_sub_f32_e32 v9, v190, v34
	v_add_f32_e32 v5, v4, v5
	v_exp_f32_e32 v9, v9
	v_sub_f32_e32 v10, v191, v34
	v_add_f32_e32 v5, v6, v5
	v_exp_f32_e32 v10, v10
	v_sub_f32_e32 v11, v196, v34
	v_add_f32_e32 v5, v7, v5
	v_exp_f32_e32 v14, v11
	v_sub_f32_e32 v11, v197, v34
	v_add_f32_e32 v5, v8, v5
	v_exp_f32_e32 v15, v11
	v_sub_f32_e32 v11, v192, v34
	v_add_f32_e32 v5, v9, v5
	v_exp_f32_e32 v16, v11
	v_sub_f32_e32 v11, v193, v34
	v_add_f32_e32 v5, v10, v5
	v_exp_f32_e32 v17, v11
	v_sub_f32_e32 v11, v188, v34
	v_add_f32_e32 v5, v14, v5
	v_exp_f32_e32 v52, v11
	v_sub_f32_e32 v11, v189, v34
	v_add_f32_e32 v5, v15, v5
	v_exp_f32_e32 v53, v11
	v_sub_f32_e32 v11, v186, v34
	v_add_f32_e32 v5, v16, v5
	v_exp_f32_e32 v54, v11
	v_sub_f32_e32 v11, v187, v34
	v_add_f32_e32 v5, v17, v5
	v_exp_f32_e32 v55, v11
	v_sub_f32_e32 v11, v114, v34
	v_add_f32_e32 v5, v52, v5
	v_exp_f32_e32 v62, v11
	v_sub_f32_e32 v11, v115, v34
	v_add_f32_e32 v5, v53, v5
	v_exp_f32_e32 v63, v11
	v_sub_f32_e32 v11, v116, v34
	v_add_f32_e32 v5, v54, v5
	v_exp_f32_e32 v64, v11
	v_sub_f32_e32 v11, v117, v34
	v_add_f32_e32 v5, v55, v5
	v_exp_f32_e32 v65, v11
	v_sub_f32_e32 v11, v118, v34
	v_add_f32_e32 v5, v62, v5
	v_exp_f32_e32 v67, v11
	v_sub_f32_e32 v11, v119, v34
	v_add_f32_e32 v5, v63, v5
	v_exp_f32_e32 v68, v11
	v_sub_f32_e32 v11, v120, v34
	v_add_f32_e32 v5, v64, v5
	v_exp_f32_e32 v69, v11
	v_sub_f32_e32 v11, v121, v34
	v_add_f32_e32 v5, v65, v5
	v_exp_f32_e32 v70, v11
	v_sub_f32_e32 v11, v122, v34
	v_add_f32_e32 v5, v67, v5
	v_exp_f32_e32 v71, v11
	v_sub_f32_e32 v11, v123, v34
	v_add_f32_e32 v5, v68, v5
	v_exp_f32_e32 v72, v11
	v_sub_f32_e32 v11, v124, v34
	v_add_f32_e32 v5, v69, v5
	v_exp_f32_e32 v73, v11
	v_sub_f32_e32 v11, v125, v34
	v_add_f32_e32 v5, v70, v5
	v_exp_f32_e32 v74, v11
	v_sub_f32_e32 v11, v150, v34
	v_add_f32_e32 v5, v71, v5
	v_exp_f32_e32 v75, v11
	v_sub_f32_e32 v11, v151, v34
	v_add_f32_e32 v5, v72, v5
	v_exp_f32_e32 v76, v11
	v_sub_f32_e32 v11, v152, v34
	v_add_f32_e32 v5, v73, v5
	v_exp_f32_e32 v77, v11
	v_sub_f32_e32 v11, v153, v34
	v_add_f32_e32 v5, v74, v5
	v_exp_f32_e32 v78, v11
	v_sub_f32_e32 v11, v154, v34
	v_add_f32_e32 v5, v75, v5
	v_exp_f32_e32 v79, v11
	v_sub_f32_e32 v11, v155, v34
	v_add_f32_e32 v5, v76, v5
	v_exp_f32_e32 v80, v11
	v_sub_f32_e32 v11, v156, v34
	v_add_f32_e32 v5, v77, v5
	v_exp_f32_e32 v81, v11
	v_sub_f32_e32 v11, v157, v34
	v_add_f32_e32 v5, v78, v5
	v_exp_f32_e32 v114, v11
	v_sub_f32_e32 v11, v158, v34
	v_add_f32_e32 v5, v79, v5
	v_exp_f32_e32 v115, v11
	v_sub_f32_e32 v11, v159, v34
	v_add_f32_e32 v5, v80, v5
	v_exp_f32_e32 v116, v11
	v_sub_f32_e32 v11, v160, v34
	v_add_f32_e32 v5, v81, v5
	v_exp_f32_e32 v117, v11
	v_sub_f32_e32 v11, v161, v34
	v_add_f32_e32 v5, v114, v5
	v_exp_f32_e32 v118, v11
	v_sub_f32_e32 v11, v162, v34
	v_add_f32_e32 v5, v115, v5
	v_exp_f32_e32 v119, v11
	v_sub_f32_e32 v11, v163, v34
	v_add_f32_e32 v5, v116, v5
	v_exp_f32_e32 v120, v11
	v_sub_f32_e32 v11, v164, v34
	v_add_f32_e32 v5, v117, v5
	v_exp_f32_e32 v121, v11
	v_sub_f32_e32 v11, v165, v34
	v_add_f32_e32 v5, v118, v5
	v_exp_f32_e32 v122, v11
	v_sub_f32_e32 v11, v166, v34
	v_add_f32_e32 v5, v119, v5
	v_exp_f32_e32 v123, v11
	v_sub_f32_e32 v11, v167, v34
	v_add_f32_e32 v5, v120, v5
	v_exp_f32_e32 v124, v11
	v_sub_f32_e32 v11, v168, v34
	v_add_f32_e32 v5, v121, v5
	v_exp_f32_e32 v125, v11
	v_sub_f32_e32 v11, v169, v34
	v_add_f32_e32 v5, v122, v5
	v_exp_f32_e32 v150, v11
	v_sub_f32_e32 v11, v170, v34
	v_add_f32_e32 v5, v123, v5
	v_exp_f32_e32 v151, v11
	v_sub_f32_e32 v11, v171, v34
	v_add_f32_e32 v5, v124, v5
	v_exp_f32_e32 v152, v11
	v_sub_f32_e32 v11, v172, v34
	v_add_f32_e32 v5, v125, v5
	v_exp_f32_e32 v153, v11
	v_sub_f32_e32 v11, v173, v34
	v_add_f32_e32 v5, v150, v5
	v_exp_f32_e32 v154, v11
	v_sub_f32_e32 v11, v176, v34
	v_add_f32_e32 v5, v151, v5
	v_exp_f32_e32 v155, v11
	v_sub_f32_e32 v11, v177, v34
	v_add_f32_e32 v5, v152, v5
	v_exp_f32_e32 v156, v11
	v_sub_f32_e32 v11, v182, v34
	v_add_f32_e32 v5, v153, v5
	v_exp_f32_e32 v157, v11
	v_sub_f32_e32 v11, v183, v34
	v_add_f32_e32 v5, v154, v5
	v_exp_f32_e32 v158, v11
	v_sub_f32_e32 v11, v184, v34
	v_add_f32_e32 v5, v155, v5
	v_exp_f32_e32 v159, v11
	v_sub_f32_e32 v11, v185, v34
	v_add_f32_e32 v5, v156, v5
	v_exp_f32_e32 v160, v11
	v_sub_f32_e32 v11, v174, v34
	v_add_f32_e32 v5, v157, v5
	v_exp_f32_e32 v161, v11
	v_add_f32_e32 v5, v158, v5
	v_add_f32_e32 v5, v159, v5
	v_add_f32_e32 v5, v160, v5
	v_add_f32_e32 v58, v161, v5
	v_cvt_pk_bf16_f32 v2, v2, v3
	v_cvt_pk_bf16_f32 v3, v4, v6
	v_cvt_pk_bf16_f32 v4, v7, v8
	v_cvt_pk_bf16_f32 v5, v9, v10
	v_lshl_add_u32 v10, s3, 6, v217
	v_add_u32_e32 v56, 0x9000, v10
	ds_read2_b64 v[6:9], v56 offset1:2
	v_sub_f32_e32 v11, v175, v34
	v_exp_f32_e32 v162, v11
	v_sub_f32_e32 v11, v180, v34
	v_exp_f32_e32 v163, v11
	v_sub_f32_e32 v11, v181, v34
	v_add_u32_e32 v59, 0xd000, v10
	v_exp_f32_e32 v164, v11
	ds_read2_b64 v[10:13], v59 offset0:32 offset1:34
	s_waitcnt lgkmcnt(1)
	v_mfma_f32_32x32x16_bf16 v[18:33], v[6:9], v[2:5], 0
	v_sub_f32_e32 v6, v178, v34
	v_cvt_pk_bf16_f32 v50, v14, v15
	v_cvt_pk_bf16_f32 v51, v16, v17
	v_cvt_pk_bf16_f32 v52, v52, v53
	v_cvt_pk_bf16_f32 v53, v54, v55
	ds_read2_b64 v[54:57], v56 offset0:4 offset1:6
	v_exp_f32_e32 v165, v6
	v_add_f32_e32 v58, v162, v58
	v_add_f32_e32 v58, v163, v58
	v_add_f32_e32 v58, v164, v58
	v_add_f32_e32 v166, v165, v58
	v_sub_f32_e32 v58, v179, v34
	v_exp_f32_e32 v167, v58
	ds_read2_b64 v[58:61], v59 offset0:36 offset1:38
	s_waitcnt lgkmcnt(2)
	v_mfma_f32_32x32x16_bf16 v[2:17], v[10:13], v[2:5], 0
	v_sub_f32_e32 v48, v48, v34
	v_sub_f32_e32 v47, v47, v34
	v_sub_f32_e32 v46, v46, v34
	v_sub_f32_e32 v45, v45, v34
	v_sub_f32_e32 v43, v43, v34
	v_sub_f32_e32 v41, v41, v34
	v_sub_f32_e32 v40, v40, v34
	s_waitcnt lgkmcnt(1)
	v_mfma_f32_32x32x16_bf16 v[18:33], v[54:57], v[50:53], v[18:33]
	v_cvt_pk_bf16_f32 v54, v62, v63
	v_cvt_pk_bf16_f32 v55, v64, v65
	v_cvt_pk_bf16_f32 v56, v67, v68
	v_lshl_add_u32 v67, s28, 6, v217
	v_add_u32_e32 v68, 0x9000, v67
	v_cvt_pk_bf16_f32 v57, v69, v70
	ds_read2_b64 v[62:65], v68 offset1:2
	s_waitcnt lgkmcnt(1)
	v_mfma_f32_32x32x16_bf16 v[2:17], v[58:61], v[50:53], v[2:17]
	v_exp_f32_e32 v69, v48
	v_sub_f32_e32 v48, v49, v34
	v_add_u32_e32 v53, 0xd000, v67
	v_exp_f32_e32 v70, v48
	ds_read2_b64 v[48:51], v53 offset0:32 offset1:34
	v_sub_f32_e32 v58, v66, v34
	v_exp_f32_e32 v66, v58
	s_waitcnt lgkmcnt(1)
	v_mfma_f32_32x32x16_bf16 v[18:33], v[62:65], v[54:57], v[18:33]
	v_cvt_pk_bf16_f32 v58, v71, v72
	v_cvt_pk_bf16_f32 v59, v73, v74
	v_cvt_pk_bf16_f32 v60, v75, v76
	v_cvt_pk_bf16_f32 v61, v77, v78
	ds_read2_b64 v[62:65], v68 offset0:4 offset1:6
	v_add_f32_e32 v52, v167, v166
	v_exp_f32_e32 v67, v47
	v_add_f32_e32 v47, v69, v52
	s_waitcnt lgkmcnt(1)
	v_mfma_f32_32x32x16_bf16 v[2:17], v[48:51], v[54:57], v[2:17]
	v_add_f32_e32 v47, v70, v47
	ds_read2_b64 v[48:51], v53 offset0:36 offset1:38
	v_add_f32_e32 v47, v66, v47
	v_add_f32_e32 v68, v67, v47
	v_lshl_add_u32 v47, s25, 6, v217
	v_add_u32_e32 v56, 0x9000, v47
	v_cvt_pk_bf16_f32 v52, v79, v80
	s_waitcnt lgkmcnt(1)
	v_mfma_f32_32x32x16_bf16 v[18:33], v[62:65], v[58:61], v[18:33]
	v_cvt_pk_bf16_f32 v53, v81, v114
	v_cvt_pk_bf16_f32 v54, v115, v116
	v_cvt_pk_bf16_f32 v55, v117, v118
	ds_read2_b64 v[62:65], v56 offset1:2
	v_add_u32_e32 v71, 0xd000, v47
	v_exp_f32_e32 v72, v40
	v_sub_f32_e32 v39, v39, v34
	s_waitcnt lgkmcnt(1)
	v_mfma_f32_32x32x16_bf16 v[2:17], v[48:51], v[58:61], v[2:17]
	v_exp_f32_e32 v60, v46
	v_exp_f32_e32 v61, v45
	v_sub_f32_e32 v48, v44, v34
	ds_read2_b64 v[44:47], v71 offset0:32 offset1:34
	v_sub_f32_e32 v38, v38, v34
	v_sub_f32_e32 v37, v37, v34
	v_sub_f32_e32 v36, v36, v34
	s_waitcnt lgkmcnt(1)
	v_mfma_f32_32x32x16_bf16 v[18:33], v[62:65], v[52:55], v[18:33]
	v_exp_f32_e32 v62, v48
	v_cvt_pk_bf16_f32 v48, v119, v120
	v_cvt_pk_bf16_f32 v49, v121, v122
	v_cvt_pk_bf16_f32 v50, v123, v124
	v_cvt_pk_bf16_f32 v51, v125, v150
	ds_read2_b64 v[56:59], v56 offset0:4 offset1:6
	v_exp_f32_e32 v63, v43
	v_add_f32_e32 v43, v60, v68
	v_add_f32_e32 v43, v61, v43
	v_add_f32_e32 v43, v62, v43
	s_waitcnt lgkmcnt(1)
	v_mfma_f32_32x32x16_bf16 v[2:17], v[44:47], v[52:55], v[2:17]
	v_add_f32_e32 v64, v63, v43
	v_sub_f32_e32 v46, v42, v34
	ds_read2_b64 v[42:45], v71 offset0:36 offset1:38
	v_lshl_add_u32 v47, s24, 6, v217
	v_add_u32_e32 v65, 0x9000, v47
	v_cvt_pk_bf16_f32 v52, v151, v152
	v_cvt_pk_bf16_f32 v53, v153, v154
	s_waitcnt lgkmcnt(1)
	v_mfma_f32_32x32x16_bf16 v[18:33], v[56:59], v[48:51], v[18:33]
	v_cvt_pk_bf16_f32 v54, v155, v156
	v_cvt_pk_bf16_f32 v55, v157, v158
	ds_read2_b64 v[56:59], v65 offset1:2
	v_add_u32_e32 v73, 0xd000, v47
	v_exp_f32_e32 v71, v41
	v_exp_f32_e32 v68, v46
	v_sub_f32_e32 v35, v35, v34
	s_waitcnt lgkmcnt(1)
	v_mfma_f32_32x32x16_bf16 v[2:17], v[42:45], v[48:51], v[2:17]
	ds_read2_b64 v[40:43], v73 offset0:32 offset1:34
	v_cvt_pk_bf16_f32 v44, v159, v160
	v_cvt_pk_bf16_f32 v45, v161, v162
	v_cvt_pk_bf16_f32 v46, v163, v164
	v_cvt_pk_bf16_f32 v47, v165, v167
	ds_read2_b64 v[48:51], v65 offset0:4 offset1:6
	v_exp_f32_e32 v35, v35
	s_waitcnt lgkmcnt(2)
	v_mfma_f32_32x32x16_bf16 v[18:33], v[56:59], v[52:55], v[18:33]
	v_exp_f32_e32 v56, v39
	v_add_f32_e32 v39, v68, v64
	v_add_f32_e32 v39, v71, v39
	v_add_f32_e32 v39, v72, v39
	v_lshl_add_u32 v57, s2, 6, v217
	v_add_u32_e32 v58, 0x9000, v57
	v_add_u32_e32 v57, 0xd000, v57
	s_waitcnt lgkmcnt(1)
	v_mfma_f32_32x32x16_bf16 v[2:17], v[40:43], v[52:55], v[2:17]
	v_add_f32_e32 v42, v56, v39
	v_exp_f32_e32 v43, v38
	ds_read2_b64 v[38:41], v73 offset0:36 offset1:38
	v_sub_f32_e32 v34, v225, v34
	s_mov_b64 s[24:25], 0x15800400
	v_add_f32_e32 v59, v43, v42
	s_waitcnt lgkmcnt(1)
	v_mfma_f32_32x32x16_bf16 v[18:33], v[48:51], v[44:47], v[18:33]
	v_cvt_pk_bf16_f32 v48, v69, v70
	v_cvt_pk_bf16_f32 v49, v66, v67
	v_cvt_pk_bf16_f32 v50, v60, v61
	v_cvt_pk_bf16_f32 v51, v62, v63
	v_exp_f32_e32 v60, v37
	v_exp_f32_e32 v61, v36
	ds_read2_b64 v[52:55], v58 offset1:2
	s_waitcnt lgkmcnt(1)
	v_mfma_f32_32x32x16_bf16 v[2:17], v[38:41], v[44:47], v[2:17]
	ds_read2_b64 v[36:39], v57 offset0:32 offset1:34
	v_cvt_pk_bf16_f32 v40, v68, v71
	v_cvt_pk_bf16_f32 v41, v72, v56
	v_cvt_pk_bf16_f32 v42, v43, v60
	v_cvt_pk_bf16_f32 v43, v61, v35
	ds_read2_b64 v[44:47], v58 offset0:4 offset1:6
	s_waitcnt lgkmcnt(1)
	v_mfma_f32_32x32x16_bf16 v[2:17], v[36:39], v[48:51], v[2:17]
	v_add_f32_e32 v36, v60, v59
	v_add_f32_e32 v36, v61, v36
	v_add_f32_e32 v38, v35, v36
	ds_bpermute_b32 v39, v129, v38
	s_waitcnt lgkmcnt(0)
	v_add_f32_e32 v38, v38, v39
	v_mfma_f32_32x32x16_bf16 v[18:33], v[52:55], v[48:51], v[18:33]
	v_exp_f32_e32 v48, v34
	ds_read2_b64 v[34:37], v57 offset0:36 offset1:38
	v_mov_b32_e32 v39, s77
	v_mfma_f32_32x32x16_bf16 v[18:33], v[44:47], v[40:43], v[18:33]
	v_add_f32_e32 v44, v48, v38
	v_div_scale_f32 v45, s[2:3], v44, v44, 1.0
	v_rcp_f32_e32 v46, v45
	v_or_b32_e32 v38, s76, v126
	v_lshlrev_b32_e32 v126, 1, v134
	s_mov_b32 s2, 0x15800000
	s_waitcnt lgkmcnt(0)
	v_mfma_f32_32x32x16_bf16 v[2:17], v[34:37], v[40:43], v[2:17]
	v_fma_f32 v34, -v45, v46, 1.0
	v_fmac_f32_e32 v46, v34, v46
	v_div_scale_f32 v34, vcc, 1.0, v44, 1.0
	v_mul_f32_e32 v35, v34, v46
	v_fma_f32 v36, -v45, v35, v34
	v_fmac_f32_e32 v35, v36, v46
	v_fma_f32 v34, -v45, v35, v34
	v_div_fmas_f32 v34, v34, v46, v35
	v_div_fixup_f32 v40, v34, v44, 1.0
	v_lshlrev_b64 v[34:35], 11, v[38:39]
	v_lshl_add_u64 v[34:35], s[74:75], 0, v[34:35]
	v_lshl_add_u64 v[34:35], v[34:35], 0, s[60:61]
	v_lshl_add_u64 v[34:35], v[34:35], 0, v[126:127]
	v_lshl_add_u64 v[36:37], v[34:35], 0, s[24:25]
	v_mbcnt_lo_u32_b32 v44, -1, 0
	v_mbcnt_hi_u32_b32 v44, -1, v44
	v_and_b32_e32 v44, 32, v44
	v_lshrrev_b32_e32 v44, 2, v44
	v_mov_b32_e32 v45, 0
	v_lshl_add_u64 v[36:37], v[36:37], 0, v[44:45]
	v_pk_mul_f32 v[18:19], v[18:19], v[40:41] op_sel_hi:[1,0]
	v_pk_mul_f32 v[20:21], v[20:21], v[40:41] op_sel_hi:[1,0]
	v_pk_mul_f32 v[22:23], v[22:23], v[40:41] op_sel_hi:[1,0]
	v_pk_mul_f32 v[24:25], v[24:25], v[40:41] op_sel_hi:[1,0]
	v_cvt_pk_bf16_f32 v18, v18, v19
	v_cvt_pk_bf16_f32 v19, v20, v21
	v_cvt_pk_bf16_f32 v20, v22, v23
	v_cvt_pk_bf16_f32 v21, v24, v25
	s_nop 1
	v_permlane32_swap_b32 v18, v20
	v_permlane32_swap_b32 v19, v21
	global_store_dwordx4 v[36:37], v[18:21], off
	v_pk_mul_f32 v[26:27], v[26:27], v[40:41] op_sel_hi:[1,0]
	v_pk_mul_f32 v[28:29], v[28:29], v[40:41] op_sel_hi:[1,0]
	v_pk_mul_f32 v[30:31], v[30:31], v[40:41] op_sel_hi:[1,0]
	v_pk_mul_f32 v[32:33], v[32:33], v[40:41] op_sel_hi:[1,0]
	v_cvt_pk_bf16_f32 v26, v26, v27
	v_cvt_pk_bf16_f32 v27, v28, v29
	v_cvt_pk_bf16_f32 v28, v30, v31
	v_cvt_pk_bf16_f32 v29, v32, v33
	s_nop 1
	v_permlane32_swap_b32 v26, v28
	v_permlane32_swap_b32 v27, v29
	global_store_dwordx4 v[36:37], v[26:29], off offset:32
	v_pk_mul_f32 v[2:3], v[2:3], v[40:41] op_sel_hi:[1,0]
	v_pk_mul_f32 v[4:5], v[4:5], v[40:41] op_sel_hi:[1,0]
	v_pk_mul_f32 v[6:7], v[6:7], v[40:41] op_sel_hi:[1,0]
	v_pk_mul_f32 v[8:9], v[8:9], v[40:41] op_sel_hi:[1,0]
	v_cvt_pk_bf16_f32 v2, v2, v3
	v_cvt_pk_bf16_f32 v3, v4, v5
	v_cvt_pk_bf16_f32 v4, v6, v7
	v_cvt_pk_bf16_f32 v5, v8, v9
	s_nop 1
	v_permlane32_swap_b32 v2, v4
	v_permlane32_swap_b32 v3, v5
	global_store_dwordx4 v[36:37], v[2:5], off offset:64
	v_pk_mul_f32 v[10:11], v[10:11], v[40:41] op_sel_hi:[1,0]
	v_pk_mul_f32 v[12:13], v[12:13], v[40:41] op_sel_hi:[1,0]
	v_pk_mul_f32 v[14:15], v[14:15], v[40:41] op_sel_hi:[1,0]
	v_pk_mul_f32 v[16:17], v[16:17], v[40:41] op_sel_hi:[1,0]
	v_cvt_pk_bf16_f32 v10, v10, v11
	v_cvt_pk_bf16_f32 v11, v12, v13
	v_cvt_pk_bf16_f32 v12, v14, v15
	v_cvt_pk_bf16_f32 v13, v16, v17
	s_nop 1
	v_permlane32_swap_b32 v10, v12
	v_permlane32_swap_b32 v11, v13
	global_store_dwordx4 v[36:37], v[10:13], off offset:96
	s_mov_b32 s3, 1
	s_andn2_b64 vcc, exec, s[22:23]
	s_cbranch_vccz .LBB0_293
